# k-scale of the expert-weight copy fetched one item ahead (counted wait leaves the stores in flight)
# baseline (speedup 1.0000x reference)
; __device__ __forceinline__ void moe_weights_ph(const int WID_, const float* __restrict__ wg, const float* __restrict__ wu, const float* __restrict__ wd, bf16* __restrict__ wgu_t, bf16* __restrict__ wd_t, char* lds, int vb, int nvb, const float* __restrict__ nw3) {
;     ...
;     float4 vn[8];
;     int it = vb * 8 + wv;
;     MW_DECODE(it);
; #pragma unroll
;     for (int i = 0; i < 8; ++i) vn[i] = *(const float4*)(sp + (size_t)(8 * i + kq) * ldw + 4 * nq);
;     for (; it < NIT; it += nvb * 8) {
;         bf16* dcur = dp; const int ldtc = ldt; const float* kcur = ksp;
;         float4 ks0 = make_float4(1.f, 1.f, 1.f, 1.f), ks1 = ks0;
;         if (kcur) { ks0 = *(const float4*)(kcur + 8 * c); ks1 = *(const float4*)(kcur + 8 * c + 4); }
; #pragma unroll
;         for (int i = 0; i < 8; ++i) { float* d = scr + (8 * i + kq) * 33 + 4 * nq; d[0] = vn[i].x; d[1] = vn[i].y; d[2] = vn[i].z; d[3] = vn[i].w; }
;         MW_DECODE(it + nvb * 8);
; #pragma unroll
;         for (int i = 0; i < 8; ++i) vn[i] = *(const float4*)(sp + (size_t)(8 * i + kq) * ldw + 4 * nq);
.LBB0_1594:
	s_or_b64 exec, exec, s[0:1]
	s_movk_i32 s0, 0x6000
	v_cmp_gt_i32_e32 vcc, s0, v8
	s_and_saveexec_b64 s[0:1], vcc
	s_cbranch_execz .LBB0_1603
	v_bfe_u32 v47, v7, 3, 3
	v_or_b32_e32 v60, 56, v47
	v_and_b32_e32 v7, 7, v7
	v_or_b32_e32 v59, 48, v47
	v_mov_b32_e32 v43, 0
	v_lshlrev_b32_e32 v42, 4, v7
	v_mul_u32_u24_e32 v1, v0, v60
	v_lshl_add_u64 v[2:3], v[4:5], 0, v[42:43]
	v_lshlrev_b32_e32 v4, 2, v1
	v_mul_u32_u24_e32 v1, v0, v59
	v_or_b32_e32 v58, 40, v47
	v_mov_b32_e32 v5, v43
	v_lshlrev_b32_e32 v8, 2, v1
	v_mov_b32_e32 v9, v43
	v_or_b32_e32 v57, 32, v47
	v_lshl_add_u64 v[4:5], v[2:3], 0, v[4:5]
	v_lshl_add_u64 v[12:13], v[2:3], 0, v[8:9]
	v_mul_u32_u24_e32 v1, v0, v58
	global_load_dwordx4 v[8:11], v[4:5], off
	s_nop 0
	global_load_dwordx4 v[12:15], v[12:13], off
	v_lshlrev_b32_e32 v4, 2, v1
	v_mul_u32_u24_e32 v1, v0, v57
	v_or_b32_e32 v56, 24, v47
	v_mov_b32_e32 v5, v43
	v_lshlrev_b32_e32 v16, 2, v1
	v_mov_b32_e32 v17, v43
	v_or_b32_e32 v55, 16, v47
	v_lshl_add_u64 v[4:5], v[2:3], 0, v[4:5]
	v_lshl_add_u64 v[20:21], v[2:3], 0, v[16:17]
	v_mul_u32_u24_e32 v1, v0, v56
	global_load_dwordx4 v[16:19], v[4:5], off
	s_nop 0
	global_load_dwordx4 v[20:23], v[20:21], off
	v_lshlrev_b32_e32 v4, 2, v1
	v_mul_u32_u24_e32 v1, v0, v55
	v_or_b32_e32 v54, 8, v47
	v_mov_b32_e32 v5, v43
	v_lshlrev_b32_e32 v24, 2, v1
	v_mov_b32_e32 v25, v43
	v_lshl_add_u64 v[4:5], v[2:3], 0, v[4:5]
	v_lshl_add_u64 v[28:29], v[2:3], 0, v[24:25]
	v_mul_u32_u24_e32 v1, v0, v54
	global_load_dwordx4 v[24:27], v[4:5], off
	s_nop 0
	global_load_dwordx4 v[28:31], v[28:29], off
	v_lshlrev_b32_e32 v4, 2, v1
	v_mov_b32_e32 v5, v43
	v_mul_u32_u24_e32 v0, v0, v47
	v_lshl_add_u64 v[4:5], v[2:3], 0, v[4:5]
	v_lshlrev_b32_e32 v0, 2, v0
	v_mov_b32_e32 v1, v43
	v_lshl_add_u64 v[0:1], v[2:3], 0, v[0:1]
	global_load_dwordx4 v[32:35], v[4:5], off
	global_load_dwordx4 v[36:39], v[0:1], off
	v_lshl_add_u32 v1, v6, 14, 0
	v_mul_u32_u24_e32 v3, 0x420, v7
	v_lshlrev_b32_e32 v4, 2, v47
	v_lshlrev_b32_e32 v0, 2, v7
	v_add_u32_e32 v2, v1, v42
	v_add3_u32 v61, v1, v3, v4
	v_mul_u32_u24_e32 v1, 0x84, v47
	v_lshlrev_b32_e32 v46, 3, v7
	v_lshl_add_u32 v63, s87, 3, v6
	s_mov_b64 s[2:3], 0
	v_add_u32_e32 v62, v2, v1
	s_movk_i32 s8, 0x1ff
	v_lshlrev_b32_e32 v42, 2, v0
	v_mov_b32_e32 v64, 13
	v_mov_b32_e32 v65, 2
	v_mov_b32_e32 v66, 5
	v_mov_b32_e32 v67, 8
	v_mov_b32_e32 v68, 6
	v_cmp_ne_u64_e32 vcc, 0, v[48:49]
	v_mov_b32_e32 v100, 1.0
	v_mov_b32_e32 v101, 1.0
	v_mov_b32_e32 v102, 1.0
	v_mov_b32_e32 v103, 1.0
	v_mov_b32_e32 v104, 1.0
	v_mov_b32_e32 v105, 1.0
	v_mov_b32_e32 v106, 1.0
	v_mov_b32_e32 v107, 1.0
	s_and_saveexec_b64 s[98:99], vcc
	v_lshlrev_b32_e32 v108, 2, v46
	v_mov_b32_e32 v109, v43
	v_lshl_add_u64 v[108:109], v[48:49], 0, v[108:109]
	global_load_dwordx4 v[100:103], v[108:109], off offset:16
	global_load_dwordx4 v[104:107], v[108:109], off
	s_or_b64 exec, exec, s[98:99]
	s_waitcnt vmcnt(0)
	s_branch .LBB0_1597
.LBB0_1596:
	s_or_b64 exec, exec, s[4:5]
	v_mul_u32_u24_e32 v11, v10, v47
	v_lshl_add_u64 v[8:9], v[12:13], 0, v[42:43]
	v_lshlrev_b32_e32 v12, 2, v11
	v_mov_b32_e32 v13, v43
	v_mul_u32_u24_e32 v11, v10, v54
	v_lshl_add_u64 v[12:13], v[8:9], 0, v[12:13]
	v_lshlrev_b32_e32 v14, 2, v11
	v_mov_b32_e32 v15, v43
	v_mul_u32_u24_e32 v11, v10, v55
	v_lshl_add_u64 v[14:15], v[8:9], 0, v[14:15]
	global_load_dwordx4 v[36:39], v[12:13], off
	global_load_dwordx4 v[32:35], v[14:15], off
	v_lshlrev_b32_e32 v12, 2, v11
	v_mov_b32_e32 v13, v43
	v_mul_u32_u24_e32 v11, v10, v56
	v_lshl_add_u64 v[12:13], v[8:9], 0, v[12:13]
	v_lshlrev_b32_e32 v14, 2, v11
	v_mov_b32_e32 v15, v43
	v_mul_u32_u24_e32 v11, v10, v57
	v_lshl_add_u64 v[14:15], v[8:9], 0, v[14:15]
	global_load_dwordx4 v[28:31], v[12:13], off
	global_load_dwordx4 v[24:27], v[14:15], off
	v_lshlrev_b32_e32 v12, 2, v11
	v_mov_b32_e32 v13, v43
	v_mul_u32_u24_e32 v11, v10, v58
	v_lshl_add_u64 v[12:13], v[8:9], 0, v[12:13]
	v_lshlrev_b32_e32 v14, 2, v11
	v_mov_b32_e32 v15, v43
	v_mul_u32_u24_e32 v11, v10, v59
	v_mul_u32_u24_e32 v10, v10, v60
	v_lshl_add_u64 v[14:15], v[8:9], 0, v[14:15]
	global_load_dwordx4 v[20:23], v[12:13], off
	global_load_dwordx4 v[16:19], v[14:15], off
	v_lshlrev_b32_e32 v12, 2, v11
	v_mov_b32_e32 v13, v43
	v_lshlrev_b32_e32 v10, 2, v10
	v_mov_b32_e32 v11, v43
	v_lshl_add_u64 v[12:13], v[8:9], 0, v[12:13]
	v_lshl_add_u64 v[8:9], v[8:9], 0, v[10:11]
	global_load_dwordx4 v[12:15], v[12:13], off
	s_nop 0
	global_load_dwordx4 v[8:11], v[8:9], off
	v_cmp_ne_u64_e32 vcc, 0, v[48:49]
	v_mov_b32_e32 v100, 1.0
	v_mov_b32_e32 v101, 1.0
	v_mov_b32_e32 v102, 1.0
	v_mov_b32_e32 v103, 1.0
	v_mov_b32_e32 v104, 1.0
	v_mov_b32_e32 v105, 1.0
	v_mov_b32_e32 v106, 1.0
	v_mov_b32_e32 v107, 1.0
	s_and_saveexec_b64 s[98:99], vcc
	v_lshlrev_b32_e32 v108, 2, v46
	v_mov_b32_e32 v109, v43
	v_lshl_add_u64 v[108:109], v[48:49], 0, v[108:109]
	global_load_dwordx4 v[100:103], v[108:109], off offset:16
	global_load_dwordx4 v[104:107], v[108:109], off
	s_or_b64 exec, exec, s[98:99]
	s_waitcnt lgkmcnt(0)
	ds_read2_b32 v[74:75], v61 offset1:8
	ds_read2_b32 v[76:77], v61 offset0:33 offset1:41
	ds_read2_b32 v[78:79], v61 offset0:66 offset1:74
	ds_read2_b32 v[80:81], v61 offset0:99 offset1:107
	ds_read2_b32 v[82:83], v61 offset0:132 offset1:140
	ds_read2_b32 v[84:85], v61 offset0:165 offset1:173
	ds_read2_b32 v[86:87], v61 offset0:198 offset1:206
	ds_read2_b32 v[88:89], v61 offset0:231 offset1:239
	v_lshlrev_b32_e32 v70, 1, v46
	v_mov_b32_e32 v71, v43
	v_lshl_add_u64 v[44:45], v[44:45], 0, v[70:71]
	s_waitcnt lgkmcnt(7)
	v_mov_b32_e32 v70, v74
	s_waitcnt lgkmcnt(6)
	v_mov_b32_e32 v71, v76
	s_waitcnt lgkmcnt(5)
	v_mov_b32_e32 v72, v78
	s_waitcnt lgkmcnt(4)
; __device__ __forceinline__ unsigned pk2(float lo, float hi) { const f32x2h v = {lo, hi}; const bf16x2h b = __builtin_convertvector(v, bf16x2h); return __builtin_bit_cast(unsigned, b); }
; __device__ __forceinline__ void moe_weights_ph(const int WID_, const float* __restrict__ wg, const float* __restrict__ wu, const float* __restrict__ wd, bf16* __restrict__ wgu_t, bf16* __restrict__ wd_t, char* lds, int vb, int nvb, const float* __restrict__ nw3) {
;     ...
;     for (; it < NIT; it += nvb * 8) {
;         bf16* dcur = dp; const int ldtc = ldt; const float* kcur = ksp;
;         float4 ks0 = make_float4(1.f, 1.f, 1.f, 1.f), ks1 = ks0;
;         if (kcur) { ks0 = *(const float4*)(kcur + 8 * c); ks1 = *(const float4*)(kcur + 8 * c + 4); }
; #pragma unroll
;         for (int i = 0; i < 8; ++i) { float* d = scr + (8 * i + kq) * 33 + 4 * nq; d[0] = vn[i].x; d[1] = vn[i].y; d[2] = vn[i].z; d[3] = vn[i].w; }
;         MW_DECODE(it + nvb * 8);
; #pragma unroll
;         for (int i = 0; i < 8; ++i) vn[i] = *(const float4*)(sp + (size_t)(8 * i + kq) * ldw + 4 * nq);
;         __builtin_amdgcn_s_waitcnt(0xc07f); asm volatile("" ::: "memory");
; #pragma unroll
;         for (int j = 0; j < 4; ++j) { const int n = (lane >> 3) + 8 * j; const float* s = scr + (8 * c) * 33 + n;
;             uint4 o; o.x = pk2(s[0 * 33] * ks0.x, s[1 * 33] * ks0.y); o.y = pk2(s[2 * 33] * ks0.z, s[3 * 33] * ks0.w); o.z = pk2(s[4 * 33] * ks1.x, s[5 * 33] * ks1.y); o.w = pk2(s[6 * 33] * ks1.z, s[7 * 33] * ks1.w);
;             *(uint4*)(dcur + (size_t)n * ldtc + 8 * c) = o; }
;         __builtin_amdgcn_s_waitcnt(0xc07f); asm volatile("" ::: "memory");
	v_mov_b32_e32 v73, v80
	v_pk_mul_f32 v[70:71], v[4:5], v[70:71]
	v_pk_mul_f32 v[72:73], v[6:7], v[72:73]
	v_cvt_pk_bf16_f32 v70, v70, v71
	v_cvt_pk_bf16_f32 v71, v72, v73
	s_waitcnt lgkmcnt(3)
	v_mov_b32_e32 v72, v82
	s_waitcnt lgkmcnt(2)
	v_mov_b32_e32 v73, v84
	s_waitcnt lgkmcnt(1)
	v_mov_b32_e32 v90, v86
	s_waitcnt lgkmcnt(0)
	v_mov_b32_e32 v91, v88
	v_pk_mul_f32 v[72:73], v[0:1], v[72:73]
	v_pk_mul_f32 v[90:91], v[2:3], v[90:91]
	v_cvt_pk_bf16_f32 v72, v72, v73
	v_cvt_pk_bf16_f32 v73, v90, v91
	v_mul_hi_i32_i24_e32 v91, v40, v47
	v_mul_i32_i24_e32 v90, v40, v47
	v_lshl_add_u64 v[90:91], v[90:91], 1, v[44:45]
	v_mov_b32_e32 v76, v75
	v_mov_b32_e32 v80, v79
	global_store_dwordx4 v[90:91], v[70:73], off
	v_mov_b32_e32 v84, v83
	v_mov_b32_e32 v88, v87
	v_pk_mul_f32 v[70:71], v[4:5], v[76:77]
	v_pk_mul_f32 v[72:73], v[6:7], v[80:81]
	v_cvt_pk_bf16_f32 v70, v70, v71
	v_cvt_pk_bf16_f32 v71, v72, v73
	v_pk_mul_f32 v[72:73], v[0:1], v[84:85]
	v_pk_mul_f32 v[74:75], v[2:3], v[88:89]
	v_cvt_pk_bf16_f32 v72, v72, v73
	v_cvt_pk_bf16_f32 v73, v74, v75
	v_mul_hi_i32_i24_e32 v75, v40, v54
	v_mul_i32_i24_e32 v74, v40, v54
	v_lshl_add_u64 v[74:75], v[74:75], 1, v[44:45]
	ds_read2_b32 v[76:77], v61 offset0:16 offset1:24
	ds_read2_b32 v[78:79], v61 offset0:49 offset1:57
	global_store_dwordx4 v[74:75], v[70:73], off
	ds_read2_b32 v[74:75], v61 offset0:82 offset1:90
	ds_read2_b32 v[80:81], v61 offset0:115 offset1:123
	ds_read2_b32 v[82:83], v61 offset0:148 offset1:156
	ds_read2_b32 v[84:85], v61 offset0:181 offset1:189
	ds_read2_b32 v[86:87], v61 offset0:214 offset1:222
	ds_read2_b32 v[88:89], v61 offset0:247 offset1:255
	s_waitcnt lgkmcnt(7)
	v_mov_b32_e32 v70, v76
	s_waitcnt lgkmcnt(6)
	v_mov_b32_e32 v71, v78
	s_waitcnt lgkmcnt(5)
	v_mov_b32_e32 v72, v74
	s_waitcnt lgkmcnt(4)
	v_mov_b32_e32 v73, v80
	v_pk_mul_f32 v[70:71], v[4:5], v[70:71]
	v_pk_mul_f32 v[72:73], v[6:7], v[72:73]
	v_cvt_pk_bf16_f32 v70, v70, v71
	v_cvt_pk_bf16_f32 v71, v72, v73
	s_waitcnt lgkmcnt(3)
	v_mov_b32_e32 v72, v82
	s_waitcnt lgkmcnt(2)
	v_mov_b32_e32 v73, v84
	v_mov_b32_e32 v78, v77
	v_mov_b32_e32 v80, v75
	v_mov_b32_e32 v84, v83
	v_pk_mul_f32 v[72:73], v[0:1], v[72:73]
	s_waitcnt lgkmcnt(1)
	v_mov_b32_e32 v90, v86
	s_waitcnt lgkmcnt(0)
	v_mov_b32_e32 v91, v88
	v_pk_mul_f32 v[4:5], v[4:5], v[78:79]
	v_pk_mul_f32 v[6:7], v[6:7], v[80:81]
	v_pk_mul_f32 v[0:1], v[0:1], v[84:85]
	v_mov_b32_e32 v88, v87
	v_pk_mul_f32 v[90:91], v[2:3], v[90:91]
	v_cvt_pk_bf16_f32 v4, v4, v5
	v_cvt_pk_bf16_f32 v5, v6, v7
	v_cvt_pk_bf16_f32 v6, v0, v1
	v_pk_mul_f32 v[0:1], v[2:3], v[88:89]
	v_cvt_pk_bf16_f32 v72, v72, v73
	v_cvt_pk_bf16_f32 v73, v90, v91
	v_mul_hi_i32_i24_e32 v91, v40, v55
	v_mul_i32_i24_e32 v90, v40, v55
	v_cvt_pk_bf16_f32 v7, v0, v1
	v_mul_hi_i32_i24_e32 v1, v40, v56
	v_mul_i32_i24_e32 v0, v40, v56
	v_lshl_add_u64 v[90:91], v[90:91], 1, v[44:45]
	v_lshl_add_u64 v[0:1], v[0:1], 1, v[44:45]
	global_store_dwordx4 v[90:91], v[70:73], off
	global_store_dwordx4 v[0:1], v[4:7], off
	s_waitcnt lgkmcnt(0)
	v_add_u32_e32 v1, 0xfffffc00, v63
	s_movk_i32 s4, 0x5bff
	v_add_u32_e32 v0, 0x400, v63
	v_cmp_lt_i32_e32 vcc, s4, v1
	s_or_b64 s[2:3], vcc, s[2:3]
	v_mov_b32_e32 v63, v0
	v_mov_b64_e32 v[44:45], v[50:51]
	v_mov_b64_e32 v[40:41], v[52:53]
	s_andn2_b64 exec, exec, s[2:3]
	s_cbranch_execz .LBB0_1603
.LBB0_1597:
	s_waitcnt vmcnt(4)
	v_mov_b32_e32 v0, v100
	v_mov_b32_e32 v1, v101
	v_mov_b32_e32 v2, v102
	v_mov_b32_e32 v3, v103
	v_mov_b32_e32 v4, v104
	v_mov_b32_e32 v5, v105
	v_mov_b32_e32 v6, v106
	v_mov_b32_e32 v7, v107
	ds_write2_b32 v62, v36, v37 offset1:1
	ds_write2_b32 v62, v38, v39 offset0:2 offset1:3
	v_add_u32_e32 v36, 0x420, v62
	ds_write2_b32 v36, v32, v33 offset1:1
	v_add_u32_e32 v32, 0x428, v62
	ds_write2_b32 v32, v34, v35 offset1:1
	v_add_u32_e32 v32, 0x840, v62
	ds_write2_b32 v32, v28, v29 offset1:1
	v_add_u32_e32 v28, 0x848, v62
	ds_write2_b32 v28, v30, v31 offset1:1
	v_add_u32_e32 v28, 0xc60, v62
	ds_write2_b32 v28, v24, v25 offset1:1
	v_add_u32_e32 v24, 0xc68, v62
	ds_write2_b32 v24, v26, v27 offset1:1
	v_add_u32_e32 v24, 0x1080, v62
	ds_write2_b32 v24, v20, v21 offset1:1
	v_add_u32_e32 v20, 0x1088, v62
	ds_write2_b32 v20, v22, v23 offset1:1
	v_add_u32_e32 v20, 0x14a0, v62
	ds_write2_b32 v20, v16, v17 offset1:1
	v_add_u32_e32 v16, 0x14a8, v62
	ds_write2_b32 v16, v18, v19 offset1:1
	v_add_u32_e32 v16, 0x18c0, v62
	ds_write2_b32 v16, v12, v13 offset1:1
	v_add_u32_e32 v12, 0x18c8, v62
	ds_write2_b32 v12, v14, v15 offset1:1
	v_add_u32_e32 v12, 0x1ce0, v62
	ds_write2_b32 v12, v8, v9 offset1:1
	v_add_u32_e32 v8, 0x1ce8, v62
	v_min_i32_e32 v9, 0x5fff, v63
	s_mov_b32 s4, 0x2aaaaaab
	ds_write2_b32 v8, v10, v11 offset1:1
	v_mul_hi_i32 v8, v9, s4
	v_lshrrev_b32_e32 v10, 31, v8
	v_ashrrev_i32_e32 v8, 7, v8
	v_add_u32_e32 v8, v8, v10
	v_mul_i32_i24_e32 v10, 0x300, v8
	v_sub_u32_e32 v14, v9, v10
	v_cmp_lt_i32_e32 vcc, s8, v14
	v_ashrrev_i32_e32 v9, 31, v8
	s_and_saveexec_b64 s[4:5], vcc
	s_xor_b64 s[4:5], exec, s[4:5]
	s_cbranch_execz .LBB0_1601
	v_lshlrev_b64 v[12:13], 21, v[8:9]
	v_lshlrev_b32_e32 v9, 5, v14
	v_and_b32_e32 v9, 0x3e0, v9
	v_add_u32_e32 v10, 0xfffffe00, v14
	v_readlane_b32 s36, v242, 15
	v_lshl_or_b32 v8, v8, 10, v9
	v_lshrrev_b32_e32 v10, 5, v10
	v_readlane_b32 s50, v242, 29
	v_readlane_b32 s51, v242, 30
	v_mov_b32_e32 v11, v43
	v_lshlrev_b32_e32 v14, 2, v9
	v_ashrrev_i32_e32 v9, 31, v8
	v_readlane_b32 s18, v242, 37
	v_lshl_add_u64 v[12:13], s[50:51], 0, v[12:13]
	v_lshlrev_b64 v[16:17], 18, v[10:11]
	v_lshlrev_b64 v[8:9], 10, v[8:9]
	v_readlane_b32 s19, v242, 38
	v_lshl_add_u64 v[12:13], v[12:13], 0, v[16:17]
	v_mov_b32_e32 v15, v43
	v_lshl_add_u64 v[8:9], s[18:19], 0, v[8:9]
	v_lshlrev_b32_e32 v10, 7, v10
	v_readlane_b32 s37, v242, 16
	v_readlane_b32 s38, v242, 17
	v_readlane_b32 s39, v242, 18
	v_readlane_b32 s40, v242, 19
	v_readlane_b32 s41, v242, 20
	v_readlane_b32 s42, v242, 21
	v_readlane_b32 s43, v242, 22
	v_readlane_b32 s44, v242, 23
	v_readlane_b32 s45, v242, 24
	v_readlane_b32 s46, v242, 25
	v_readlane_b32 s47, v242, 26
	v_readlane_b32 s48, v242, 27
	v_readlane_b32 s49, v242, 28
	v_lshl_add_u64 v[12:13], v[12:13], 0, v[14:15]
	v_lshl_add_u64 v[50:51], v[8:9], 0, v[10:11]
